# speedup vs baseline: 1.0063x; 1.0063x over previous
_Z8dog_mainPKfS0_S0_S0_S0_S0_S0_Pf:
	s_load_dwordx8 s[12:19], s[0:1], 0x0
	s_load_dwordx8 s[20:27], s[0:1], 0x20
	s_and_b32 s3, s2, 7
	s_lshl_b32 s3, s3, 5
	s_lshr_b32 s4, s2, 3
	s_add_i32 s4, s3, s4
	s_and_b32 s6, s4, 3
	s_lshr_b32 s7, s4, 2
	s_mov_b32 s5, 0
	s_lshl_b64 s[8:9], s[4:5], 18
	v_and_b32_e32 v1, 63, v0
	v_lshrrev_b32_e32 v2, 6, v0
	v_and_b32_e32 v3, 31, v0
	v_lshl_or_b32 v4, v2, 5, v3
	v_lshlrev_b32_e32 v5, 2, v4
	v_lshlrev_b32_e32 v6, 4, v1
	v_lshl_or_b32 v6, v2, 15, v6
	v_bfe_u32 v7, v0, 5, 1
	s_waitcnt lgkmcnt(0)
	s_add_u32 s12, s12, s8
	s_addc_u32 s13, s13, s9
	v_lshlrev_b32_e32 v6, 4, v1
	v_bfe_u32 v16, v2, 0, 1
	v_lshl_or_b32 v6, v16, 12, v6
	v_bfe_u32 v16, v2, 1, 1
	v_lshl_or_b32 v6, v16, 13, v6
	v_bfe_u32 v16, v2, 2, 1
	v_lshl_or_b32 v6, v16, 14, v6
	global_load_dwordx4 v[128:131], v6, s[12:13] nt
	global_load_dwordx4 v[132:135], v6, s[12:13] offset:1024 nt
	global_load_dwordx4 v[136:139], v6, s[12:13] offset:2048 nt
	global_load_dwordx4 v[140:143], v6, s[12:13] offset:3072 nt
	global_load_dword v20, v5, s[18:19]
	global_load_dword v21, v5, s[20:21]
	global_load_dword v22, v5, s[22:23]
	global_load_dword v23, v5, s[24:25]
	global_load_dword v24, v5, s[14:15]
	global_load_dword v25, v5, s[16:17]
	v_add_u32_e32 v17, 0x8000, v6
	global_load_dwordx4 v[144:147], v17, s[12:13] nt
	v_add_u32_e32 v17, 0x8400, v6
	global_load_dwordx4 v[148:151], v17, s[12:13] nt
	v_add_u32_e32 v17, 0x8800, v6
	global_load_dwordx4 v[152:155], v17, s[12:13] nt
	v_add_u32_e32 v17, 0x8c00, v6
	global_load_dwordx4 v[156:159], v17, s[12:13] nt
	v_add_u32_e32 v17, 0x10000, v6
	global_load_dwordx4 v[160:163], v17, s[12:13] nt
	v_add_u32_e32 v17, 0x10400, v6
	global_load_dwordx4 v[164:167], v17, s[12:13] nt
	v_add_u32_e32 v17, 0x10800, v6
	global_load_dwordx4 v[168:171], v17, s[12:13] nt
	v_add_u32_e32 v17, 0x10c00, v6
	global_load_dwordx4 v[172:175], v17, s[12:13] nt
	v_add_u32_e32 v17, 0x18000, v6
	global_load_dwordx4 v[176:179], v17, s[12:13] nt
	v_add_u32_e32 v17, 0x18400, v6
	global_load_dwordx4 v[180:183], v17, s[12:13] nt
	v_add_u32_e32 v17, 0x18800, v6
	global_load_dwordx4 v[184:187], v17, s[12:13] nt
	v_add_u32_e32 v17, 0x18c00, v6
	global_load_dwordx4 v[188:191], v17, s[12:13] nt
	v_add_u32_e32 v17, 0x20000, v6
	global_load_dwordx4 v[192:195], v17, s[12:13] nt
	v_add_u32_e32 v17, 0x20400, v6
	global_load_dwordx4 v[196:199], v17, s[12:13] nt
	v_add_u32_e32 v17, 0x20800, v6
	global_load_dwordx4 v[200:203], v17, s[12:13] nt
	v_add_u32_e32 v17, 0x20c00, v6
	global_load_dwordx4 v[204:207], v17, s[12:13] nt
	v_add_u32_e32 v17, 0x28000, v6
	global_load_dwordx4 v[208:211], v17, s[12:13] nt
	v_add_u32_e32 v17, 0x28400, v6
	global_load_dwordx4 v[212:215], v17, s[12:13] nt
	v_add_u32_e32 v17, 0x28800, v6
	global_load_dwordx4 v[216:219], v17, s[12:13] nt
	v_add_u32_e32 v17, 0x28c00, v6
	global_load_dwordx4 v[220:223], v17, s[12:13] nt
	v_add_u32_e32 v17, 0x30000, v6
	global_load_dwordx4 v[224:227], v17, s[12:13] nt
	v_add_u32_e32 v17, 0x30400, v6
	global_load_dwordx4 v[228:231], v17, s[12:13] nt
	v_add_u32_e32 v17, 0x30800, v6
	global_load_dwordx4 v[232:235], v17, s[12:13] nt
	v_add_u32_e32 v17, 0x30c00, v6
	global_load_dwordx4 v[236:239], v17, s[12:13] nt
	v_add_u32_e32 v17, 0x38000, v6
	global_load_dwordx4 v[240:243], v17, s[12:13] nt
	v_add_u32_e32 v17, 0x38400, v6
	global_load_dwordx4 v[244:247], v17, s[12:13] nt
	v_add_u32_e32 v17, 0x38800, v6
	global_load_dwordx4 v[248:251], v17, s[12:13] nt
	v_add_u32_e32 v17, 0x38c00, v6
	global_load_dwordx4 v[252:255], v17, s[12:13] nt
	v_and_b32_e32 v16, 1, v0
	v_cmp_eq_u32_e64 s[30:31], 0, v16
	v_and_b32_e32 v17, 2, v0
	v_cmp_eq_u32_e64 s[32:33], 0, v17
	v_lshrrev_b32_e32 v17, 2, v1
	v_lshlrev_b32_e32 v14, 1, v17
	v_bfe_u32 v16, v2, 0, 1
	s_movk_i32 s10, 0x80
	v_mad_u32_u24 v14, v16, s10, v14
	v_bfe_u32 v16, v2, 1, 1
	s_movk_i32 s10, 0x110
	v_mad_u32_u24 v14, v16, s10, v14
	v_bfe_u32 v16, v2, 2, 1
	s_movk_i32 s10, 0x220
	v_mad_u32_u24 v14, v16, s10, v14
	v_bfe_u32 v16, v0, 0, 1
	s_movk_i32 s10, 0x20
	v_mad_u32_u24 v14, v16, s10, v14
	v_bfe_u32 v16, v0, 1, 1
	s_movk_i32 s10, 0x40
	v_mad_u32_u24 v14, v16, s10, v14
	s_movk_i32 s10, 0x110
	v_lshlrev_b32_e32 v17, 4, v7
	v_mad_u32_u24 v15, v3, s10, v17
	s_lshl_b32 s11, s6, 5
	v_lshl_add_u32 v18, v7, 2, s11
	v_cvt_f32_u32_e32 v18, v18
	v_lshlrev_b32_e32 v19, 3, v7
	v_cvt_f32_u32_e32 v19, v19
	s_waitcnt vmcnt(28)
	v_add_f32_e32 v26, v20, v21
	v_rcp_f32_e32 v27, v20
	v_rcp_f32_e32 v28, v26
	v_sub_f32_e32 v12, v19, v22
	v_sub_f32_e32 v13, v18, v23
	v_fma_f32 v29, -v20, v27, 1.0
	v_fma_f32 v30, -v26, v28, 1.0
	v_fma_f32 v27, v29, v27, v27
	v_fma_f32 v28, v30, v28, v28
	v_mul_f32_e32 v8, 0xbf38aa3b, v27
	v_mul_f32_e32 v9, 0xbf38aa3b, v28
	v_mul_f32_e32 v29, v24, v27
	v_mul_f32_e32 v30, v25, v28
	v_mul_f32_e32 v10, 0x3e22f983, v29
	v_mul_f32_e32 v11, 0x3e22f983, v30
	v_mul_f32_e32 v16, v12, v12
	v_add_f32_e32 v17, 0x3f800000, v12
	v_add_f32_e32 v18, 0x40000000, v12
	v_add_f32_e32 v19, 0x40400000, v12
	v_mul_f32_e32 v17, v17, v17
	v_mul_f32_e32 v18, v18, v18
	v_mul_f32_e32 v19, v19, v19
	v_mul_f32_e32 v20, v8, v16
	v_mul_f32_e32 v24, v9, v16
	v_mul_f32_e32 v21, v8, v17
	v_mul_f32_e32 v25, v9, v17
	v_mul_f32_e32 v22, v8, v18
	v_mul_f32_e32 v26, v9, v18
	v_mul_f32_e32 v23, v8, v19
	v_mul_f32_e32 v27, v9, v19
	v_exp_f32_e32 v20, v20
	v_exp_f32_e32 v21, v21
	v_exp_f32_e32 v22, v22
	v_exp_f32_e32 v23, v23
	v_exp_f32_e32 v24, v24
	v_exp_f32_e32 v25, v25
	v_exp_f32_e32 v26, v26
	v_exp_f32_e32 v27, v27
	v_cvt_pk_f16_f32 v32, v20, v21
	v_cvt_pk_f16_f32 v33, v22, v23
	v_cvt_pk_f16_f32 v64, v24, v25
	v_cvt_pk_f16_f32 v65, v26, v27
	v_add_f32_e32 v16, 0x40800000, v12
	v_add_f32_e32 v17, 0x40a00000, v12
	v_add_f32_e32 v18, 0x40c00000, v12
	v_add_f32_e32 v19, 0x40e00000, v12
	v_mul_f32_e32 v16, v16, v16
	v_mul_f32_e32 v17, v17, v17
	v_mul_f32_e32 v18, v18, v18
	v_mul_f32_e32 v19, v19, v19
	v_mul_f32_e32 v20, v8, v16
	v_mul_f32_e32 v24, v9, v16
	v_mul_f32_e32 v21, v8, v17
	v_mul_f32_e32 v25, v9, v17
	v_mul_f32_e32 v22, v8, v18
	v_mul_f32_e32 v26, v9, v18
	v_mul_f32_e32 v23, v8, v19
	v_mul_f32_e32 v27, v9, v19
	v_exp_f32_e32 v20, v20
	v_exp_f32_e32 v21, v21
	v_exp_f32_e32 v22, v22
	v_exp_f32_e32 v23, v23
	v_exp_f32_e32 v24, v24
	v_exp_f32_e32 v25, v25
	v_exp_f32_e32 v26, v26
	v_exp_f32_e32 v27, v27
	v_cvt_pk_f16_f32 v34, v20, v21
	v_cvt_pk_f16_f32 v35, v22, v23
	v_cvt_pk_f16_f32 v66, v24, v25
	v_cvt_pk_f16_f32 v67, v26, v27
	v_add_f32_e32 v16, 0x41800000, v12
	v_add_f32_e32 v17, 0x41880000, v12
	v_add_f32_e32 v18, 0x41900000, v12
	v_add_f32_e32 v19, 0x41980000, v12
	v_mul_f32_e32 v16, v16, v16
	v_mul_f32_e32 v17, v17, v17
	v_mul_f32_e32 v18, v18, v18
	v_mul_f32_e32 v19, v19, v19
	v_mul_f32_e32 v20, v8, v16
	v_mul_f32_e32 v24, v9, v16
	v_mul_f32_e32 v21, v8, v17
	v_mul_f32_e32 v25, v9, v17
	v_mul_f32_e32 v22, v8, v18
	v_mul_f32_e32 v26, v9, v18
	v_mul_f32_e32 v23, v8, v19
	v_mul_f32_e32 v27, v9, v19
	v_exp_f32_e32 v20, v20
	v_exp_f32_e32 v21, v21
	v_exp_f32_e32 v22, v22
	v_exp_f32_e32 v23, v23
	v_exp_f32_e32 v24, v24
	v_exp_f32_e32 v25, v25
	v_exp_f32_e32 v26, v26
	v_exp_f32_e32 v27, v27
	v_cvt_pk_f16_f32 v36, v20, v21
	v_cvt_pk_f16_f32 v37, v22, v23
	v_cvt_pk_f16_f32 v68, v24, v25
	v_cvt_pk_f16_f32 v69, v26, v27
	v_add_f32_e32 v16, 0x41a00000, v12
	v_add_f32_e32 v17, 0x41a80000, v12
	v_add_f32_e32 v18, 0x41b00000, v12
	v_add_f32_e32 v19, 0x41b80000, v12
	v_mul_f32_e32 v16, v16, v16
	v_mul_f32_e32 v17, v17, v17
	v_mul_f32_e32 v18, v18, v18
	v_mul_f32_e32 v19, v19, v19
	v_mul_f32_e32 v20, v8, v16
	v_mul_f32_e32 v24, v9, v16
	v_mul_f32_e32 v21, v8, v17
	v_mul_f32_e32 v25, v9, v17
	v_mul_f32_e32 v22, v8, v18
	v_mul_f32_e32 v26, v9, v18
	v_mul_f32_e32 v23, v8, v19
	v_mul_f32_e32 v27, v9, v19
	v_exp_f32_e32 v20, v20
	v_exp_f32_e32 v21, v21
	v_exp_f32_e32 v22, v22
	v_exp_f32_e32 v23, v23
	v_exp_f32_e32 v24, v24
	v_exp_f32_e32 v25, v25
	v_exp_f32_e32 v26, v26
	v_exp_f32_e32 v27, v27
	v_cvt_pk_f16_f32 v38, v20, v21
	v_cvt_pk_f16_f32 v39, v22, v23
	v_cvt_pk_f16_f32 v70, v24, v25
	v_cvt_pk_f16_f32 v71, v26, v27
	v_add_f32_e32 v16, 0x42000000, v12
	v_add_f32_e32 v17, 0x42040000, v12
	v_add_f32_e32 v18, 0x42080000, v12
	v_add_f32_e32 v19, 0x420c0000, v12
	v_mul_f32_e32 v16, v16, v16
	v_mul_f32_e32 v17, v17, v17
	v_mul_f32_e32 v18, v18, v18
	v_mul_f32_e32 v19, v19, v19
	v_mul_f32_e32 v20, v8, v16
	v_mul_f32_e32 v24, v9, v16
	v_mul_f32_e32 v21, v8, v17
	v_mul_f32_e32 v25, v9, v17
	v_mul_f32_e32 v22, v8, v18
	v_mul_f32_e32 v26, v9, v18
	v_mul_f32_e32 v23, v8, v19
	v_mul_f32_e32 v27, v9, v19
	v_exp_f32_e32 v20, v20
	v_exp_f32_e32 v21, v21
	v_exp_f32_e32 v22, v22
	v_exp_f32_e32 v23, v23
	v_exp_f32_e32 v24, v24
	v_exp_f32_e32 v25, v25
	v_exp_f32_e32 v26, v26
	v_exp_f32_e32 v27, v27
	v_cvt_pk_f16_f32 v40, v20, v21
	v_cvt_pk_f16_f32 v41, v22, v23
	v_cvt_pk_f16_f32 v72, v24, v25
	v_cvt_pk_f16_f32 v73, v26, v27
	v_add_f32_e32 v16, 0x42100000, v12
	v_add_f32_e32 v17, 0x42140000, v12
	v_add_f32_e32 v18, 0x42180000, v12
	v_add_f32_e32 v19, 0x421c0000, v12
	v_mul_f32_e32 v16, v16, v16
	v_mul_f32_e32 v17, v17, v17
	v_mul_f32_e32 v18, v18, v18
	v_mul_f32_e32 v19, v19, v19
	v_mul_f32_e32 v20, v8, v16
	v_mul_f32_e32 v24, v9, v16
	v_mul_f32_e32 v21, v8, v17
	v_mul_f32_e32 v25, v9, v17
	v_mul_f32_e32 v22, v8, v18
	v_mul_f32_e32 v26, v9, v18
	v_mul_f32_e32 v23, v8, v19
	v_mul_f32_e32 v27, v9, v19
	v_exp_f32_e32 v20, v20
	v_exp_f32_e32 v21, v21
	v_exp_f32_e32 v22, v22
	v_exp_f32_e32 v23, v23
	v_exp_f32_e32 v24, v24
	v_exp_f32_e32 v25, v25
	v_exp_f32_e32 v26, v26
	v_exp_f32_e32 v27, v27
	v_cvt_pk_f16_f32 v42, v20, v21
	v_cvt_pk_f16_f32 v43, v22, v23
	v_cvt_pk_f16_f32 v74, v24, v25
	v_cvt_pk_f16_f32 v75, v26, v27
	v_add_f32_e32 v16, 0x42400000, v12
	v_add_f32_e32 v17, 0x42440000, v12
	v_add_f32_e32 v18, 0x42480000, v12
	v_add_f32_e32 v19, 0x424c0000, v12
	v_mul_f32_e32 v16, v16, v16
	v_mul_f32_e32 v17, v17, v17
	v_mul_f32_e32 v18, v18, v18
	v_mul_f32_e32 v19, v19, v19
	v_mul_f32_e32 v20, v8, v16
	v_mul_f32_e32 v24, v9, v16
	v_mul_f32_e32 v21, v8, v17
	v_mul_f32_e32 v25, v9, v17
	v_mul_f32_e32 v22, v8, v18
	v_mul_f32_e32 v26, v9, v18
	v_mul_f32_e32 v23, v8, v19
	v_mul_f32_e32 v27, v9, v19
	v_exp_f32_e32 v20, v20
	v_exp_f32_e32 v21, v21
	v_exp_f32_e32 v22, v22
	v_exp_f32_e32 v23, v23
	v_exp_f32_e32 v24, v24
	v_exp_f32_e32 v25, v25
	v_exp_f32_e32 v26, v26
	v_exp_f32_e32 v27, v27
	v_cvt_pk_f16_f32 v44, v20, v21
	v_cvt_pk_f16_f32 v45, v22, v23
	v_cvt_pk_f16_f32 v76, v24, v25
	v_cvt_pk_f16_f32 v77, v26, v27
	v_add_f32_e32 v16, 0x42500000, v12
	v_add_f32_e32 v17, 0x42540000, v12
	v_add_f32_e32 v18, 0x42580000, v12
	v_add_f32_e32 v19, 0x425c0000, v12
	v_mul_f32_e32 v16, v16, v16
	v_mul_f32_e32 v17, v17, v17
	v_mul_f32_e32 v18, v18, v18
	v_mul_f32_e32 v19, v19, v19
	v_mul_f32_e32 v20, v8, v16
	v_mul_f32_e32 v24, v9, v16
	v_mul_f32_e32 v21, v8, v17
	v_mul_f32_e32 v25, v9, v17
	v_mul_f32_e32 v22, v8, v18
	v_mul_f32_e32 v26, v9, v18
	v_mul_f32_e32 v23, v8, v19
	v_mul_f32_e32 v27, v9, v19
	v_exp_f32_e32 v20, v20
	v_exp_f32_e32 v21, v21
	v_exp_f32_e32 v22, v22
	v_exp_f32_e32 v23, v23
	v_exp_f32_e32 v24, v24
	v_exp_f32_e32 v25, v25
	v_exp_f32_e32 v26, v26
	v_exp_f32_e32 v27, v27
	v_cvt_pk_f16_f32 v46, v20, v21
	v_cvt_pk_f16_f32 v47, v22, v23
	v_cvt_pk_f16_f32 v78, v24, v25
	v_cvt_pk_f16_f32 v79, v26, v27
	v_add_f32_e32 v16, 0x42800000, v12
	v_add_f32_e32 v17, 0x42820000, v12
	v_add_f32_e32 v18, 0x42840000, v12
	v_add_f32_e32 v19, 0x42860000, v12
	v_mul_f32_e32 v16, v16, v16
	v_mul_f32_e32 v17, v17, v17
	v_mul_f32_e32 v18, v18, v18
	v_mul_f32_e32 v19, v19, v19
	v_mul_f32_e32 v20, v8, v16
	v_mul_f32_e32 v24, v9, v16
	v_mul_f32_e32 v21, v8, v17
	v_mul_f32_e32 v25, v9, v17
	v_mul_f32_e32 v22, v8, v18
	v_mul_f32_e32 v26, v9, v18
	v_mul_f32_e32 v23, v8, v19
	v_mul_f32_e32 v27, v9, v19
	v_exp_f32_e32 v20, v20
	v_exp_f32_e32 v21, v21
	v_exp_f32_e32 v22, v22
	v_exp_f32_e32 v23, v23
	v_exp_f32_e32 v24, v24
	v_exp_f32_e32 v25, v25
	v_exp_f32_e32 v26, v26
	v_exp_f32_e32 v27, v27
	v_cvt_pk_f16_f32 v48, v20, v21
	v_cvt_pk_f16_f32 v49, v22, v23
	v_cvt_pk_f16_f32 v80, v24, v25
	v_cvt_pk_f16_f32 v81, v26, v27
	v_add_f32_e32 v16, 0x42880000, v12
	v_add_f32_e32 v17, 0x428a0000, v12
	v_add_f32_e32 v18, 0x428c0000, v12
	v_add_f32_e32 v19, 0x428e0000, v12
	v_mul_f32_e32 v16, v16, v16
	v_mul_f32_e32 v17, v17, v17
	v_mul_f32_e32 v18, v18, v18
	v_mul_f32_e32 v19, v19, v19
	v_mul_f32_e32 v20, v8, v16
	v_mul_f32_e32 v24, v9, v16
	v_mul_f32_e32 v21, v8, v17
	v_mul_f32_e32 v25, v9, v17
	v_mul_f32_e32 v22, v8, v18
	v_mul_f32_e32 v26, v9, v18
	v_mul_f32_e32 v23, v8, v19
	v_mul_f32_e32 v27, v9, v19
	v_exp_f32_e32 v20, v20
	v_exp_f32_e32 v21, v21
	v_exp_f32_e32 v22, v22
	v_exp_f32_e32 v23, v23
	v_exp_f32_e32 v24, v24
	v_exp_f32_e32 v25, v25
	v_exp_f32_e32 v26, v26
	v_exp_f32_e32 v27, v27
	v_cvt_pk_f16_f32 v50, v20, v21
	v_cvt_pk_f16_f32 v51, v22, v23
	v_cvt_pk_f16_f32 v82, v24, v25
	v_cvt_pk_f16_f32 v83, v26, v27
	v_add_f32_e32 v16, 0x42a00000, v12
	v_add_f32_e32 v17, 0x42a20000, v12
	v_add_f32_e32 v18, 0x42a40000, v12
	v_add_f32_e32 v19, 0x42a60000, v12
	v_mul_f32_e32 v16, v16, v16
	v_mul_f32_e32 v17, v17, v17
	v_mul_f32_e32 v18, v18, v18
	v_mul_f32_e32 v19, v19, v19
	v_mul_f32_e32 v20, v8, v16
	v_mul_f32_e32 v24, v9, v16
	v_mul_f32_e32 v21, v8, v17
	v_mul_f32_e32 v25, v9, v17
	v_mul_f32_e32 v22, v8, v18
	v_mul_f32_e32 v26, v9, v18
	v_mul_f32_e32 v23, v8, v19
	v_mul_f32_e32 v27, v9, v19
	v_exp_f32_e32 v20, v20
	v_exp_f32_e32 v21, v21
	v_exp_f32_e32 v22, v22
	v_exp_f32_e32 v23, v23
	v_exp_f32_e32 v24, v24
	v_exp_f32_e32 v25, v25
	v_exp_f32_e32 v26, v26
	v_exp_f32_e32 v27, v27
	v_cvt_pk_f16_f32 v52, v20, v21
	v_cvt_pk_f16_f32 v53, v22, v23
	v_cvt_pk_f16_f32 v84, v24, v25
	v_cvt_pk_f16_f32 v85, v26, v27
	v_add_f32_e32 v16, 0x42a80000, v12
	v_add_f32_e32 v17, 0x42aa0000, v12
	v_add_f32_e32 v18, 0x42ac0000, v12
	v_add_f32_e32 v19, 0x42ae0000, v12
	v_mul_f32_e32 v16, v16, v16
	v_mul_f32_e32 v17, v17, v17
	v_mul_f32_e32 v18, v18, v18
	v_mul_f32_e32 v19, v19, v19
	v_mul_f32_e32 v20, v8, v16
	v_mul_f32_e32 v24, v9, v16
	v_mul_f32_e32 v21, v8, v17
	v_mul_f32_e32 v25, v9, v17
	v_mul_f32_e32 v22, v8, v18
	v_mul_f32_e32 v26, v9, v18
	v_mul_f32_e32 v23, v8, v19
	v_mul_f32_e32 v27, v9, v19
	v_exp_f32_e32 v20, v20
	v_exp_f32_e32 v21, v21
	v_exp_f32_e32 v22, v22
	v_exp_f32_e32 v23, v23
	v_exp_f32_e32 v24, v24
	v_exp_f32_e32 v25, v25
	v_exp_f32_e32 v26, v26
	v_exp_f32_e32 v27, v27
	v_cvt_pk_f16_f32 v54, v20, v21
	v_cvt_pk_f16_f32 v55, v22, v23
	v_cvt_pk_f16_f32 v86, v24, v25
	v_cvt_pk_f16_f32 v87, v26, v27
	v_add_f32_e32 v16, 0x42c00000, v12
	v_add_f32_e32 v17, 0x42c20000, v12
	v_add_f32_e32 v18, 0x42c40000, v12
	v_add_f32_e32 v19, 0x42c60000, v12
	v_mul_f32_e32 v16, v16, v16
	v_mul_f32_e32 v17, v17, v17
	v_mul_f32_e32 v18, v18, v18
	v_mul_f32_e32 v19, v19, v19
	v_mul_f32_e32 v20, v8, v16
	v_mul_f32_e32 v24, v9, v16
	v_mul_f32_e32 v21, v8, v17
	v_mul_f32_e32 v25, v9, v17
	v_mul_f32_e32 v22, v8, v18
	v_mul_f32_e32 v26, v9, v18
	v_mul_f32_e32 v23, v8, v19
	v_mul_f32_e32 v27, v9, v19
	v_exp_f32_e32 v20, v20
	v_exp_f32_e32 v21, v21
	v_exp_f32_e32 v22, v22
	v_exp_f32_e32 v23, v23
	v_exp_f32_e32 v24, v24
	v_exp_f32_e32 v25, v25
	v_exp_f32_e32 v26, v26
	v_exp_f32_e32 v27, v27
	v_cvt_pk_f16_f32 v56, v20, v21
	v_cvt_pk_f16_f32 v57, v22, v23
	v_cvt_pk_f16_f32 v88, v24, v25
	v_cvt_pk_f16_f32 v89, v26, v27
	v_add_f32_e32 v16, 0x42c80000, v12
	v_add_f32_e32 v17, 0x42ca0000, v12
	v_add_f32_e32 v18, 0x42cc0000, v12
	v_add_f32_e32 v19, 0x42ce0000, v12
	v_mul_f32_e32 v16, v16, v16
	v_mul_f32_e32 v17, v17, v17
	v_mul_f32_e32 v18, v18, v18
	v_mul_f32_e32 v19, v19, v19
	v_mul_f32_e32 v20, v8, v16
	v_mul_f32_e32 v24, v9, v16
	v_mul_f32_e32 v21, v8, v17
	v_mul_f32_e32 v25, v9, v17
	v_mul_f32_e32 v22, v8, v18
	v_mul_f32_e32 v26, v9, v18
	v_mul_f32_e32 v23, v8, v19
	v_mul_f32_e32 v27, v9, v19
	v_exp_f32_e32 v20, v20
	v_exp_f32_e32 v21, v21
	v_exp_f32_e32 v22, v22
	v_exp_f32_e32 v23, v23
	v_exp_f32_e32 v24, v24
	v_exp_f32_e32 v25, v25
	v_exp_f32_e32 v26, v26
	v_exp_f32_e32 v27, v27
	v_cvt_pk_f16_f32 v58, v20, v21
	v_cvt_pk_f16_f32 v59, v22, v23
	v_cvt_pk_f16_f32 v90, v24, v25
	v_cvt_pk_f16_f32 v91, v26, v27
	v_add_f32_e32 v16, 0x42e00000, v12
	v_add_f32_e32 v17, 0x42e20000, v12
	v_add_f32_e32 v18, 0x42e40000, v12
	v_add_f32_e32 v19, 0x42e60000, v12
	v_mul_f32_e32 v16, v16, v16
	v_mul_f32_e32 v17, v17, v17
	v_mul_f32_e32 v18, v18, v18
	v_mul_f32_e32 v19, v19, v19
	v_mul_f32_e32 v20, v8, v16
	v_mul_f32_e32 v24, v9, v16
	v_mul_f32_e32 v21, v8, v17
	v_mul_f32_e32 v25, v9, v17
	v_mul_f32_e32 v22, v8, v18
	v_mul_f32_e32 v26, v9, v18
	v_mul_f32_e32 v23, v8, v19
	v_mul_f32_e32 v27, v9, v19
	v_exp_f32_e32 v20, v20
	v_exp_f32_e32 v21, v21
	v_exp_f32_e32 v22, v22
	v_exp_f32_e32 v23, v23
	v_exp_f32_e32 v24, v24
	v_exp_f32_e32 v25, v25
	v_exp_f32_e32 v26, v26
	v_exp_f32_e32 v27, v27
	v_cvt_pk_f16_f32 v60, v20, v21
	v_cvt_pk_f16_f32 v61, v22, v23
	v_cvt_pk_f16_f32 v92, v24, v25
	v_cvt_pk_f16_f32 v93, v26, v27
	v_add_f32_e32 v16, 0x42e80000, v12
	v_add_f32_e32 v17, 0x42ea0000, v12
	v_add_f32_e32 v18, 0x42ec0000, v12
	v_add_f32_e32 v19, 0x42ee0000, v12
	v_mul_f32_e32 v16, v16, v16
	v_mul_f32_e32 v17, v17, v17
	v_mul_f32_e32 v18, v18, v18
	v_mul_f32_e32 v19, v19, v19
	v_mul_f32_e32 v20, v8, v16
	v_mul_f32_e32 v24, v9, v16
	v_mul_f32_e32 v21, v8, v17
	v_mul_f32_e32 v25, v9, v17
	v_mul_f32_e32 v22, v8, v18
	v_mul_f32_e32 v26, v9, v18
	v_mul_f32_e32 v23, v8, v19
	v_mul_f32_e32 v27, v9, v19
	v_exp_f32_e32 v20, v20
	v_exp_f32_e32 v21, v21
	v_exp_f32_e32 v22, v22
	v_exp_f32_e32 v23, v23
	v_exp_f32_e32 v24, v24
	v_exp_f32_e32 v25, v25
	v_exp_f32_e32 v26, v26
	v_exp_f32_e32 v27, v27
	v_cvt_pk_f16_f32 v62, v20, v21
	v_cvt_pk_f16_f32 v63, v22, v23
	v_cvt_pk_f16_f32 v94, v24, v25
	v_cvt_pk_f16_f32 v95, v26, v27
	v_mul_f32_e32 v16, v13, v13
	v_add_f32_e32 v17, 0x3f800000, v13
	v_add_f32_e32 v18, 0x40000000, v13
	v_add_f32_e32 v19, 0x40400000, v13
	v_mul_f32_e32 v17, v17, v17
	v_mul_f32_e32 v18, v18, v18
	v_mul_f32_e32 v19, v19, v19
	v_mul_f32_e32 v20, v8, v16
	v_mul_f32_e32 v24, v9, v16
	v_mul_f32_e32 v21, v8, v17
	v_mul_f32_e32 v25, v9, v17
	v_mul_f32_e32 v22, v8, v18
	v_mul_f32_e32 v26, v9, v18
	v_mul_f32_e32 v23, v8, v19
	v_mul_f32_e32 v27, v9, v19
	v_exp_f32_e32 v20, v20
	v_exp_f32_e32 v21, v21
	v_exp_f32_e32 v22, v22
	v_exp_f32_e32 v23, v23
	v_exp_f32_e32 v24, v24
	v_exp_f32_e32 v25, v25
	v_exp_f32_e32 v26, v26
	v_exp_f32_e32 v27, v27
	v_mul_f32_e32 v96, v10, v20
	v_mul_f32_e32 v97, v10, v21
	v_mul_f32_e32 v98, v10, v22
	v_mul_f32_e32 v99, v10, v23
	v_mul_f32_e32 v112, v11, v24
	v_mul_f32_e32 v113, v11, v25
	v_mul_f32_e32 v114, v11, v26
	v_mul_f32_e32 v115, v11, v27
	v_add_f32_e32 v16, 0x41000000, v13
	v_add_f32_e32 v17, 0x41100000, v13
	v_add_f32_e32 v18, 0x41200000, v13
	v_add_f32_e32 v19, 0x41300000, v13
	v_mul_f32_e32 v16, v16, v16
	v_mul_f32_e32 v17, v17, v17
	v_mul_f32_e32 v18, v18, v18
	v_mul_f32_e32 v19, v19, v19
	v_mul_f32_e32 v20, v8, v16
	v_mul_f32_e32 v24, v9, v16
	v_mul_f32_e32 v21, v8, v17
	v_mul_f32_e32 v25, v9, v17
	v_mul_f32_e32 v22, v8, v18
	v_mul_f32_e32 v26, v9, v18
	v_mul_f32_e32 v23, v8, v19
	v_mul_f32_e32 v27, v9, v19
	v_exp_f32_e32 v20, v20
	v_exp_f32_e32 v21, v21
	v_exp_f32_e32 v22, v22
	v_exp_f32_e32 v23, v23
	v_exp_f32_e32 v24, v24
	v_exp_f32_e32 v25, v25
	v_exp_f32_e32 v26, v26
	v_exp_f32_e32 v27, v27
	v_mul_f32_e32 v100, v10, v20
	v_mul_f32_e32 v101, v10, v21
	v_mul_f32_e32 v102, v10, v22
	v_mul_f32_e32 v103, v10, v23
	v_mul_f32_e32 v116, v11, v24
	v_mul_f32_e32 v117, v11, v25
	v_mul_f32_e32 v118, v11, v26
	v_mul_f32_e32 v119, v11, v27
	v_add_f32_e32 v16, 0x41800000, v13
	v_add_f32_e32 v17, 0x41880000, v13
	v_add_f32_e32 v18, 0x41900000, v13
	v_add_f32_e32 v19, 0x41980000, v13
	v_mul_f32_e32 v16, v16, v16
	v_mul_f32_e32 v17, v17, v17
	v_mul_f32_e32 v18, v18, v18
	v_mul_f32_e32 v19, v19, v19
	v_mul_f32_e32 v20, v8, v16
	v_mul_f32_e32 v24, v9, v16
	v_mul_f32_e32 v21, v8, v17
	v_mul_f32_e32 v25, v9, v17
	v_mul_f32_e32 v22, v8, v18
	v_mul_f32_e32 v26, v9, v18
	v_mul_f32_e32 v23, v8, v19
	v_mul_f32_e32 v27, v9, v19
	v_exp_f32_e32 v20, v20
	v_exp_f32_e32 v21, v21
	v_exp_f32_e32 v22, v22
	v_exp_f32_e32 v23, v23
	v_exp_f32_e32 v24, v24
	v_exp_f32_e32 v25, v25
	v_exp_f32_e32 v26, v26
	v_exp_f32_e32 v27, v27
	v_mul_f32_e32 v104, v10, v20
	v_mul_f32_e32 v105, v10, v21
	v_mul_f32_e32 v106, v10, v22
	v_mul_f32_e32 v107, v10, v23
	v_mul_f32_e32 v120, v11, v24
	v_mul_f32_e32 v121, v11, v25
	v_mul_f32_e32 v122, v11, v26
	v_mul_f32_e32 v123, v11, v27
	v_add_f32_e32 v16, 0x41c00000, v13
	v_add_f32_e32 v17, 0x41c80000, v13
	v_add_f32_e32 v18, 0x41d00000, v13
	v_add_f32_e32 v19, 0x41d80000, v13
	v_mul_f32_e32 v16, v16, v16
	v_mul_f32_e32 v17, v17, v17
	v_mul_f32_e32 v18, v18, v18
	v_mul_f32_e32 v19, v19, v19
	v_mul_f32_e32 v20, v8, v16
	v_mul_f32_e32 v24, v9, v16
	v_mul_f32_e32 v21, v8, v17
	v_mul_f32_e32 v25, v9, v17
	v_mul_f32_e32 v22, v8, v18
	v_mul_f32_e32 v26, v9, v18
	v_mul_f32_e32 v23, v8, v19
	v_mul_f32_e32 v27, v9, v19
	v_exp_f32_e32 v20, v20
	v_exp_f32_e32 v21, v21
	v_exp_f32_e32 v22, v22
	v_exp_f32_e32 v23, v23
	v_exp_f32_e32 v24, v24
	v_exp_f32_e32 v25, v25
	v_exp_f32_e32 v26, v26
	v_exp_f32_e32 v27, v27
	v_mul_f32_e32 v108, v10, v20
	v_mul_f32_e32 v109, v10, v21
	v_mul_f32_e32 v110, v10, v22
	v_mul_f32_e32 v111, v10, v23
	v_mul_f32_e32 v124, v11, v24
	v_mul_f32_e32 v125, v11, v25
	v_mul_f32_e32 v126, v11, v26
	v_mul_f32_e32 v127, v11, v27
	s_waitcnt vmcnt(28)
	v_add_f32_e32 v128, v128, v129
	v_add_f32_e32 v130, v130, v131
	v_add_f32_e32 v132, v132, v133
	v_add_f32_e32 v134, v134, v135
	v_add_f32_e32 v136, v136, v137
	v_add_f32_e32 v138, v138, v139
	v_add_f32_e32 v140, v140, v141
	v_add_f32_e32 v142, v142, v143
	v_add_f32_e32 v128, v128, v130
	v_add_f32_e32 v132, v132, v134
	v_add_f32_e32 v136, v136, v138
	v_add_f32_e32 v140, v140, v142
	v_cndmask_b32_e64 v130, v128, v132, s[30:31]
	v_cndmask_b32_e64 v134, v136, v140, s[30:31]
	v_cndmask_b32_e64 v129, v132, v128, s[30:31]
	v_cndmask_b32_e64 v133, v140, v136, s[30:31]
	v_add_f32_dpp v129, v130, v129 quad_perm:[1,0,3,2] row_mask:0xf bank_mask:0xf bound_ctrl:1
	v_add_f32_dpp v133, v134, v133 quad_perm:[1,0,3,2] row_mask:0xf bank_mask:0xf bound_ctrl:1
	v_cndmask_b32_e64 v135, v129, v133, s[32:33]
	v_cndmask_b32_e64 v131, v133, v129, s[32:33]
	s_nop 1
	v_add_f32_dpp v131, v135, v131 quad_perm:[2,3,0,1] row_mask:0xf bank_mask:0xf bound_ctrl:1
	v_cvt_f16_f32_e32 v131, v131
	ds_write_b16 v14, v131 offset:0
	s_waitcnt vmcnt(24)
	v_add_f32_e32 v144, v144, v145
	v_add_f32_e32 v146, v146, v147
	v_add_f32_e32 v148, v148, v149
	v_add_f32_e32 v150, v150, v151
	v_add_f32_e32 v152, v152, v153
	v_add_f32_e32 v154, v154, v155
	v_add_f32_e32 v156, v156, v157
	v_add_f32_e32 v158, v158, v159
	v_add_f32_e32 v144, v144, v146
	v_add_f32_e32 v148, v148, v150
	v_add_f32_e32 v152, v152, v154
	v_add_f32_e32 v156, v156, v158
	v_cndmask_b32_e64 v146, v144, v148, s[30:31]
	v_cndmask_b32_e64 v150, v152, v156, s[30:31]
	v_cndmask_b32_e64 v145, v148, v144, s[30:31]
	v_cndmask_b32_e64 v149, v156, v152, s[30:31]
	v_add_f32_dpp v145, v146, v145 quad_perm:[1,0,3,2] row_mask:0xf bank_mask:0xf bound_ctrl:1
	v_add_f32_dpp v149, v150, v149 quad_perm:[1,0,3,2] row_mask:0xf bank_mask:0xf bound_ctrl:1
	v_cndmask_b32_e64 v151, v145, v149, s[32:33]
	v_cndmask_b32_e64 v147, v149, v145, s[32:33]
	s_nop 1
	v_add_f32_dpp v147, v151, v147 quad_perm:[2,3,0,1] row_mask:0xf bank_mask:0xf bound_ctrl:1
	v_cvt_f16_f32_e32 v147, v147
	ds_write_b16 v14, v147 offset:1088
	s_waitcnt vmcnt(20)
	v_add_f32_e32 v160, v160, v161
	v_add_f32_e32 v162, v162, v163
	v_add_f32_e32 v164, v164, v165
	v_add_f32_e32 v166, v166, v167
	v_add_f32_e32 v168, v168, v169
	v_add_f32_e32 v170, v170, v171
	v_add_f32_e32 v172, v172, v173
	v_add_f32_e32 v174, v174, v175
	v_add_f32_e32 v160, v160, v162
	v_add_f32_e32 v164, v164, v166
	v_add_f32_e32 v168, v168, v170
	v_add_f32_e32 v172, v172, v174
	v_cndmask_b32_e64 v162, v160, v164, s[30:31]
	v_cndmask_b32_e64 v166, v168, v172, s[30:31]
	v_cndmask_b32_e64 v161, v164, v160, s[30:31]
	v_cndmask_b32_e64 v165, v172, v168, s[30:31]
	v_add_f32_dpp v161, v162, v161 quad_perm:[1,0,3,2] row_mask:0xf bank_mask:0xf bound_ctrl:1
	v_add_f32_dpp v165, v166, v165 quad_perm:[1,0,3,2] row_mask:0xf bank_mask:0xf bound_ctrl:1
	v_cndmask_b32_e64 v167, v161, v165, s[32:33]
	v_cndmask_b32_e64 v163, v165, v161, s[32:33]
	s_nop 1
	v_add_f32_dpp v163, v167, v163 quad_perm:[2,3,0,1] row_mask:0xf bank_mask:0xf bound_ctrl:1
	v_cvt_f16_f32_e32 v163, v163
	ds_write_b16 v14, v163 offset:2176
	s_waitcnt vmcnt(16)
	v_add_f32_e32 v176, v176, v177
	v_add_f32_e32 v178, v178, v179
	v_add_f32_e32 v180, v180, v181
	v_add_f32_e32 v182, v182, v183
	v_add_f32_e32 v184, v184, v185
	v_add_f32_e32 v186, v186, v187
	v_add_f32_e32 v188, v188, v189
	v_add_f32_e32 v190, v190, v191
	v_add_f32_e32 v176, v176, v178
	v_add_f32_e32 v180, v180, v182
	v_add_f32_e32 v184, v184, v186
	v_add_f32_e32 v188, v188, v190
	v_cndmask_b32_e64 v178, v176, v180, s[30:31]
	v_cndmask_b32_e64 v182, v184, v188, s[30:31]
	v_cndmask_b32_e64 v177, v180, v176, s[30:31]
	v_cndmask_b32_e64 v181, v188, v184, s[30:31]
	v_add_f32_dpp v177, v178, v177 quad_perm:[1,0,3,2] row_mask:0xf bank_mask:0xf bound_ctrl:1
	v_add_f32_dpp v181, v182, v181 quad_perm:[1,0,3,2] row_mask:0xf bank_mask:0xf bound_ctrl:1
	v_cndmask_b32_e64 v183, v177, v181, s[32:33]
	v_cndmask_b32_e64 v179, v181, v177, s[32:33]
	s_nop 1
	v_add_f32_dpp v179, v183, v179 quad_perm:[2,3,0,1] row_mask:0xf bank_mask:0xf bound_ctrl:1
	v_cvt_f16_f32_e32 v179, v179
	ds_write_b16 v14, v179 offset:3264
	s_waitcnt vmcnt(12)
	v_add_f32_e32 v192, v192, v193
	v_add_f32_e32 v194, v194, v195
	v_add_f32_e32 v196, v196, v197
	v_add_f32_e32 v198, v198, v199
	v_add_f32_e32 v200, v200, v201
	v_add_f32_e32 v202, v202, v203
	v_add_f32_e32 v204, v204, v205
	v_add_f32_e32 v206, v206, v207
	v_add_f32_e32 v192, v192, v194
	v_add_f32_e32 v196, v196, v198
	v_add_f32_e32 v200, v200, v202
	v_add_f32_e32 v204, v204, v206
	v_cndmask_b32_e64 v194, v192, v196, s[30:31]
	v_cndmask_b32_e64 v198, v200, v204, s[30:31]
	v_cndmask_b32_e64 v193, v196, v192, s[30:31]
	v_cndmask_b32_e64 v197, v204, v200, s[30:31]
	v_add_f32_dpp v193, v194, v193 quad_perm:[1,0,3,2] row_mask:0xf bank_mask:0xf bound_ctrl:1
	v_add_f32_dpp v197, v198, v197 quad_perm:[1,0,3,2] row_mask:0xf bank_mask:0xf bound_ctrl:1
	v_cndmask_b32_e64 v199, v193, v197, s[32:33]
	v_cndmask_b32_e64 v195, v197, v193, s[32:33]
	s_nop 1
	v_add_f32_dpp v195, v199, v195 quad_perm:[2,3,0,1] row_mask:0xf bank_mask:0xf bound_ctrl:1
	v_cvt_f16_f32_e32 v195, v195
	ds_write_b16 v14, v195 offset:4352
	s_waitcnt vmcnt(8)
	v_add_f32_e32 v208, v208, v209
	v_add_f32_e32 v210, v210, v211
	v_add_f32_e32 v212, v212, v213
	v_add_f32_e32 v214, v214, v215
	v_add_f32_e32 v216, v216, v217
	v_add_f32_e32 v218, v218, v219
	v_add_f32_e32 v220, v220, v221
	v_add_f32_e32 v222, v222, v223
	v_add_f32_e32 v208, v208, v210
	v_add_f32_e32 v212, v212, v214
	v_add_f32_e32 v216, v216, v218
	v_add_f32_e32 v220, v220, v222
	v_cndmask_b32_e64 v210, v208, v212, s[30:31]
	v_cndmask_b32_e64 v214, v216, v220, s[30:31]
	v_cndmask_b32_e64 v209, v212, v208, s[30:31]
	v_cndmask_b32_e64 v213, v220, v216, s[30:31]
	v_add_f32_dpp v209, v210, v209 quad_perm:[1,0,3,2] row_mask:0xf bank_mask:0xf bound_ctrl:1
	v_add_f32_dpp v213, v214, v213 quad_perm:[1,0,3,2] row_mask:0xf bank_mask:0xf bound_ctrl:1
	v_cndmask_b32_e64 v215, v209, v213, s[32:33]
	v_cndmask_b32_e64 v211, v213, v209, s[32:33]
	s_nop 1
	v_add_f32_dpp v211, v215, v211 quad_perm:[2,3,0,1] row_mask:0xf bank_mask:0xf bound_ctrl:1
	v_cvt_f16_f32_e32 v211, v211
	ds_write_b16 v14, v211 offset:5440
	s_waitcnt vmcnt(4)
	v_add_f32_e32 v224, v224, v225
	v_add_f32_e32 v226, v226, v227
	v_add_f32_e32 v228, v228, v229
	v_add_f32_e32 v230, v230, v231
	v_add_f32_e32 v232, v232, v233
	v_add_f32_e32 v234, v234, v235
	v_add_f32_e32 v236, v236, v237
	v_add_f32_e32 v238, v238, v239
	v_add_f32_e32 v224, v224, v226
	v_add_f32_e32 v228, v228, v230
	v_add_f32_e32 v232, v232, v234
	v_add_f32_e32 v236, v236, v238
	v_cndmask_b32_e64 v226, v224, v228, s[30:31]
	v_cndmask_b32_e64 v230, v232, v236, s[30:31]
	v_cndmask_b32_e64 v225, v228, v224, s[30:31]
	v_cndmask_b32_e64 v229, v236, v232, s[30:31]
	v_add_f32_dpp v225, v226, v225 quad_perm:[1,0,3,2] row_mask:0xf bank_mask:0xf bound_ctrl:1
	v_add_f32_dpp v229, v230, v229 quad_perm:[1,0,3,2] row_mask:0xf bank_mask:0xf bound_ctrl:1
	v_cndmask_b32_e64 v231, v225, v229, s[32:33]
	v_cndmask_b32_e64 v227, v229, v225, s[32:33]
	s_nop 1
	v_add_f32_dpp v227, v231, v227 quad_perm:[2,3,0,1] row_mask:0xf bank_mask:0xf bound_ctrl:1
	v_cvt_f16_f32_e32 v227, v227
	ds_write_b16 v14, v227 offset:6528
	s_waitcnt vmcnt(0)
	v_add_f32_e32 v240, v240, v241
	v_add_f32_e32 v242, v242, v243
	v_add_f32_e32 v244, v244, v245
	v_add_f32_e32 v246, v246, v247
	v_add_f32_e32 v248, v248, v249
	v_add_f32_e32 v250, v250, v251
	v_add_f32_e32 v252, v252, v253
	v_add_f32_e32 v254, v254, v255
	v_add_f32_e32 v240, v240, v242
	v_add_f32_e32 v244, v244, v246
	v_add_f32_e32 v248, v248, v250
	v_add_f32_e32 v252, v252, v254
	v_cndmask_b32_e64 v242, v240, v244, s[30:31]
	v_cndmask_b32_e64 v246, v248, v252, s[30:31]
	v_cndmask_b32_e64 v241, v244, v240, s[30:31]
	v_cndmask_b32_e64 v245, v252, v248, s[30:31]
	v_add_f32_dpp v241, v242, v241 quad_perm:[1,0,3,2] row_mask:0xf bank_mask:0xf bound_ctrl:1
	v_add_f32_dpp v245, v246, v245 quad_perm:[1,0,3,2] row_mask:0xf bank_mask:0xf bound_ctrl:1
	v_cndmask_b32_e64 v247, v241, v245, s[32:33]
	v_cndmask_b32_e64 v243, v245, v241, s[32:33]
	s_nop 1
	v_add_f32_dpp v243, v247, v243 quad_perm:[2,3,0,1] row_mask:0xf bank_mask:0xf bound_ctrl:1
	v_cvt_f16_f32_e32 v243, v243
	ds_write_b16 v14, v243 offset:7616
	s_waitcnt lgkmcnt(0)
	s_barrier
	ds_read_b128 v[160:163], v15 offset:0
	ds_read_b128 v[164:167], v15 offset:32
	ds_read_b128 v[168:171], v15 offset:64
	ds_read_b128 v[172:175], v15 offset:96
	ds_read_b128 v[176:179], v15 offset:128
	ds_read_b128 v[180:183], v15 offset:160
	ds_read_b128 v[184:187], v15 offset:192
	ds_read_b128 v[188:191], v15 offset:224
	s_waitcnt lgkmcnt(7)
	v_mfma_f32_32x32x16_f16 v[128:143], v[160:163], v[32:35], 0
	v_mfma_f32_32x32x16_f16 v[144:159], v[160:163], v[64:67], 0
	s_waitcnt lgkmcnt(6)
	v_mfma_f32_32x32x16_f16 v[128:143], v[164:167], v[36:39], v[128:143]
	v_mfma_f32_32x32x16_f16 v[144:159], v[164:167], v[68:71], v[144:159]
	s_waitcnt lgkmcnt(5)
	v_mfma_f32_32x32x16_f16 v[128:143], v[168:171], v[40:43], v[128:143]
	v_mfma_f32_32x32x16_f16 v[144:159], v[168:171], v[72:75], v[144:159]
	s_waitcnt lgkmcnt(4)
	v_mfma_f32_32x32x16_f16 v[128:143], v[172:175], v[44:47], v[128:143]
	v_mfma_f32_32x32x16_f16 v[144:159], v[172:175], v[76:79], v[144:159]
	s_waitcnt lgkmcnt(3)
	v_mfma_f32_32x32x16_f16 v[128:143], v[176:179], v[48:51], v[128:143]
	v_mfma_f32_32x32x16_f16 v[144:159], v[176:179], v[80:83], v[144:159]
	s_waitcnt lgkmcnt(2)
	v_mfma_f32_32x32x16_f16 v[128:143], v[180:183], v[52:55], v[128:143]
	v_mfma_f32_32x32x16_f16 v[144:159], v[180:183], v[84:87], v[144:159]
	s_waitcnt lgkmcnt(1)
	v_mfma_f32_32x32x16_f16 v[128:143], v[184:187], v[56:59], v[128:143]
	v_mfma_f32_32x32x16_f16 v[144:159], v[184:187], v[88:91], v[144:159]
	s_waitcnt lgkmcnt(0)
	v_mfma_f32_32x32x16_f16 v[128:143], v[188:191], v[60:63], v[128:143]
	v_mfma_f32_32x32x16_f16 v[144:159], v[188:191], v[92:95], v[144:159]
	s_nop 15
	s_nop 3
	v_mul_f32_e32 v16, v96, v128
	v_mul_f32_e32 v17, v97, v129
	v_mul_f32_e32 v18, v98, v130
	v_mul_f32_e32 v19, v99, v131
	v_fma_f32 v16, -v112, v144, v16
	v_fma_f32 v17, -v113, v145, v17
	v_fma_f32 v18, -v114, v146, v18
	v_fma_f32 v19, -v115, v147, v19
	v_fma_f32 v16, v100, v132, v16
	v_fma_f32 v16, -v116, v148, v16
	v_fma_f32 v17, v101, v133, v17
	v_fma_f32 v17, -v117, v149, v17
	v_fma_f32 v18, v102, v134, v18
	v_fma_f32 v18, -v118, v150, v18
	v_fma_f32 v19, v103, v135, v19
	v_fma_f32 v19, -v119, v151, v19
	v_fma_f32 v16, v104, v136, v16
	v_fma_f32 v16, -v120, v152, v16
	v_fma_f32 v17, v105, v137, v17
	v_fma_f32 v17, -v121, v153, v17
	v_fma_f32 v18, v106, v138, v18
	v_fma_f32 v18, -v122, v154, v18
	v_fma_f32 v19, v107, v139, v19
	v_fma_f32 v19, -v123, v155, v19
	v_fma_f32 v16, v108, v140, v16
	v_fma_f32 v16, -v124, v156, v16
	v_fma_f32 v17, v109, v141, v17
	v_fma_f32 v17, -v125, v157, v17
	v_fma_f32 v18, v110, v142, v18
	v_fma_f32 v18, -v126, v158, v18
	v_fma_f32 v19, v111, v143, v19
	v_fma_f32 v19, -v127, v159, v19
	v_add_f32_e32 v16, v16, v17
	v_add_f32_e32 v18, v18, v19
	v_add_f32_e32 v16, v16, v18
	v_mov_b32_e32 v17, v16
	s_lshl_b32 s6, s6, 6
	s_add_i32 s6, s6, s7
	s_lshl_b32 s6, s6, 10
	v_permlane32_swap_b32_e32 v16, v17
	v_add_u32_e32 v5, s6, v5
	v_cmp_gt_u32_e32 vcc, 32, v1
	v_add_f32_e32 v16, v16, v17
	s_and_saveexec_b64 s[2:3], vcc
	s_cbranch_execz .Ldog_main_done
	global_store_dword v5, v16, s[26:27]
